# weight-conversion pools: the first-iteration wait ladder before the LDS writes replaced by one wait at the end of the prologue (steady-state iterations no longer wait on the previous iteration's store
# baseline (speedup 1.0000x reference)
; DI CvItem cv_decode(const Params& P, int it) { CvItem c; int item;
;     if (it < NE * CV_GU1) { const int e = it / CV_GU1; c.W = P.in[I_WGU] + (size_t)e * D * 4096; c.N = 4096; c.WT = (unsigned char*)(P.ws + WS_WGU) + (size_t)e * 4096 * D; c.kind = 2; item = it % CV_GU1; }
;     else { const int r = it - NE * CV_GU1; const int e = r / CV_DN1; c.W = P.in[I_WDN] + (size_t)e * D * D; c.N = D; c.WT = (unsigned char*)(P.ws + WS_WDN) + (size_t)e * D * D; c.kind = 3; item = r % CV_DN1; }
;     const int nblk = c.N / 32, kb = item / nblk, nb = item % nblk; c.k0 = 128 * kb; c.n0 = 32 * nb; return c; }
; DI void cv_issue(const CvItem& c, int lane, f32x4 (&v)[16]) { const int c4 = (lane & 7) * 4, r8 = lane >> 3;
; #pragma unroll
;     for (int i = 0; i < 16; ++i) v[i] = *(const f32x4*)(c.W + (size_t)(c.k0 + 8 * i + r8) * c.N + c.n0 + c4); }
; DI void conv_pool(const Params& P, LAS unsigned char* lds, int pool, int blk_lo, int blk_hi) {
;     ...
;     auto claim = [&]() -> int { unsigned v_ = 0u; if (lane == 0) v_ = __hip_atomic_fetch_add(ctr, 1u, __ATOMIC_RELAXED, __HIP_MEMORY_SCOPE_AGENT); return blk_lo + (int)__builtin_amdgcn_readfirstlane(v_); };
;     const int blk = claim(); if (blk >= CV_NBLK) return;
;     int it = blk * CV_BLK, left = CV_BLK;
;     CvItem cur = cv_decode(P, it); f32x4 v[16]; cv_issue(cur, lane, v);
.LBB0_368:
	s_lshr_b32 s13, s16, 5
	s_sext_i32_i16 s2, s10
	v_cvt_f32_ubyte0_e32 v1, s13
	v_cvt_f32_i32_e32 v0, s2
	v_rcp_iflag_f32_e32 v2, v1
	s_mulk_i32 s12, 0x4200
	s_ashr_i32 s2, s2, 30
	s_add_i32 s33, s12, 0
	v_mul_f32_e32 v2, v0, v2
	v_trunc_f32_e32 v2, v2
	v_fma_f32 v0, -v2, v1, v0
	v_cvt_i32_f32_e32 v2, v2
	s_or_b32 s12, s2, 1
	v_cmp_ge_f32_e64 s[2:3], |v0|, v1
	s_and_b64 s[2:3], s[2:3], exec
	s_cselect_b32 s2, s12, 0
	v_readfirstlane_b32 s3, v2
	s_add_i32 s2, s3, s2
	s_sext_i32_i16 s3, s2
	s_mul_i32 s2, s2, s13
	s_sub_i32 s2, s10, s2
	v_ashrrev_i32_e32 v132, 3, v56
	s_sext_i32_i16 s2, s2
	s_lshl_b32 s10, s3, 7
	v_lshlrev_b32_e32 v0, 2, v56
	v_add_u32_e32 v133, 8, v132
	v_add_u32_e32 v134, 16, v132
	v_add_u32_e32 v135, 24, v132
	v_add_u32_e32 v136, 32, v132
	v_add_u32_e32 v137, 40, v132
	v_add_u32_e32 v138, 48, v132
	v_add_u32_e32 v139, 56, v132
	v_add_u32_e32 v140, 64, v132
	v_add_u32_e32 v141, 0x48, v132
	v_add_u32_e32 v142, 0x50, v132
	v_add_u32_e32 v143, 0x58, v132
	v_add_u32_e32 v144, 0x60, v132
	v_add_u32_e32 v145, 0x68, v132
	v_add_u32_e32 v146, 0x70, v132
	s_lshl_b32 s12, s2, 5
	v_and_b32_e32 v58, 28, v0
	v_add_u32_e32 v0, s10, v132
	v_add_u32_e32 v2, s10, v133
	v_add_u32_e32 v8, s10, v134
	v_add_u32_e32 v10, s10, v135
	v_add_u32_e32 v16, s10, v136
	v_add_u32_e32 v18, s10, v137
	v_add_u32_e32 v24, s10, v138
	v_add_u32_e32 v26, s10, v139
	v_add_u32_e32 v32, s10, v140
	v_add_u32_e32 v34, s10, v141
	v_add_u32_e32 v40, s10, v142
	v_add_u32_e32 v42, s10, v143
	v_add_u32_e32 v48, s10, v144
	v_add_u32_e32 v50, s10, v145
	v_add_u32_e32 v57, s10, v146
	v_add_u32_e32 v147, 0x78, v132
	v_mad_i64_i32 v[0:1], s[2:3], v0, s16, 0
	s_ashr_i32 s13, s12, 31
	v_mad_i64_i32 v[2:3], s[22:23], v2, s16, 0
	v_mad_i64_i32 v[8:9], s[22:23], v8, s16, 0
	v_mad_i64_i32 v[10:11], s[22:23], v10, s16, 0
	v_mad_i64_i32 v[16:17], s[22:23], v16, s16, 0
	v_mad_i64_i32 v[18:19], s[22:23], v18, s16, 0
	v_mad_i64_i32 v[24:25], s[22:23], v24, s16, 0
	v_mad_i64_i32 v[26:27], s[22:23], v26, s16, 0
	v_mad_i64_i32 v[32:33], s[22:23], v32, s16, 0
	v_mad_i64_i32 v[34:35], s[22:23], v34, s16, 0
	v_mad_i64_i32 v[40:41], s[22:23], v40, s16, 0
	v_mad_i64_i32 v[42:43], s[22:23], v42, s16, 0
	v_mad_i64_i32 v[48:49], s[22:23], v48, s16, 0
	v_mad_i64_i32 v[50:51], s[22:23], v50, s16, 0
	v_mad_i64_i32 v[60:61], s[22:23], v57, s16, 0
	v_add_u32_e32 v57, s10, v147
	v_lshl_add_u64 v[0:1], v[0:1], 2, s[14:15]
	s_lshl_b64 s[2:3], s[12:13], 2
	v_lshl_add_u64 v[2:3], v[2:3], 2, s[14:15]
	v_lshl_add_u64 v[8:9], v[8:9], 2, s[14:15]
	v_lshl_add_u64 v[10:11], v[10:11], 2, s[14:15]
	v_lshl_add_u64 v[16:17], v[16:17], 2, s[14:15]
	v_lshl_add_u64 v[18:19], v[18:19], 2, s[14:15]
	v_lshl_add_u64 v[24:25], v[24:25], 2, s[14:15]
	v_lshl_add_u64 v[26:27], v[26:27], 2, s[14:15]
	v_lshl_add_u64 v[32:33], v[32:33], 2, s[14:15]
	v_lshl_add_u64 v[34:35], v[34:35], 2, s[14:15]
	v_lshl_add_u64 v[40:41], v[40:41], 2, s[14:15]
	v_lshl_add_u64 v[42:43], v[42:43], 2, s[14:15]
	v_lshl_add_u64 v[48:49], v[48:49], 2, s[14:15]
	v_lshl_add_u64 v[50:51], v[50:51], 2, s[14:15]
	v_lshl_add_u64 v[60:61], v[60:61], 2, s[14:15]
	v_mad_i64_i32 v[62:63], s[16:17], v57, s16, 0
	v_mov_b32_e32 v129, 0
	v_lshl_add_u64 v[0:1], v[0:1], 0, s[2:3]
	v_lshlrev_b32_e32 v128, 2, v58
	v_lshl_add_u64 v[2:3], v[2:3], 0, s[2:3]
	v_lshl_add_u64 v[8:9], v[8:9], 0, s[2:3]
	v_lshl_add_u64 v[10:11], v[10:11], 0, s[2:3]
	v_lshl_add_u64 v[16:17], v[16:17], 0, s[2:3]
	v_lshl_add_u64 v[18:19], v[18:19], 0, s[2:3]
	v_lshl_add_u64 v[24:25], v[24:25], 0, s[2:3]
	v_lshl_add_u64 v[26:27], v[26:27], 0, s[2:3]
	v_lshl_add_u64 v[32:33], v[32:33], 0, s[2:3]
	v_lshl_add_u64 v[34:35], v[34:35], 0, s[2:3]
	v_lshl_add_u64 v[40:41], v[40:41], 0, s[2:3]
	v_lshl_add_u64 v[42:43], v[42:43], 0, s[2:3]
	v_lshl_add_u64 v[48:49], v[48:49], 0, s[2:3]
	v_lshl_add_u64 v[50:51], v[50:51], 0, s[2:3]
	v_lshl_add_u64 v[60:61], v[60:61], 0, s[2:3]
	v_lshl_add_u64 v[62:63], v[62:63], 2, s[14:15]
	v_lshl_add_u64 v[0:1], v[0:1], 0, v[128:129]
	v_lshl_add_u64 v[2:3], v[2:3], 0, v[128:129]
	v_lshl_add_u64 v[8:9], v[8:9], 0, v[128:129]
	v_lshl_add_u64 v[10:11], v[10:11], 0, v[128:129]
	v_lshl_add_u64 v[16:17], v[16:17], 0, v[128:129]
	v_lshl_add_u64 v[18:19], v[18:19], 0, v[128:129]
	v_lshl_add_u64 v[24:25], v[24:25], 0, v[128:129]
	v_lshl_add_u64 v[26:27], v[26:27], 0, v[128:129]
	v_lshl_add_u64 v[32:33], v[32:33], 0, v[128:129]
	v_lshl_add_u64 v[34:35], v[34:35], 0, v[128:129]
	v_lshl_add_u64 v[40:41], v[40:41], 0, v[128:129]
	v_lshl_add_u64 v[42:43], v[42:43], 0, v[128:129]
	v_lshl_add_u64 v[48:49], v[48:49], 0, v[128:129]
	v_lshl_add_u64 v[50:51], v[50:51], 0, v[128:129]
	v_lshl_add_u64 v[60:61], v[60:61], 0, v[128:129]
	v_lshl_add_u64 v[62:63], v[62:63], 0, s[2:3]
	global_load_dwordx4 v[4:7], v[0:1], off nt
	s_nop 0
	global_load_dwordx4 v[0:3], v[2:3], off nt
	s_nop 0
	global_load_dwordx4 v[12:15], v[8:9], off nt
	s_nop 0
	global_load_dwordx4 v[8:11], v[10:11], off nt
	s_nop 0
	global_load_dwordx4 v[20:23], v[16:17], off nt
	s_nop 0
	global_load_dwordx4 v[16:19], v[18:19], off nt
	s_nop 0
	global_load_dwordx4 v[28:31], v[24:25], off nt
	s_nop 0
	global_load_dwordx4 v[24:27], v[26:27], off nt
	s_nop 0
	global_load_dwordx4 v[36:39], v[32:33], off nt
	s_nop 0
	global_load_dwordx4 v[32:35], v[34:35], off nt
	s_nop 0
	global_load_dwordx4 v[44:47], v[40:41], off nt
	s_nop 0
	global_load_dwordx4 v[40:43], v[42:43], off nt
	s_nop 0
	global_load_dwordx4 v[52:55], v[48:49], off nt
	s_nop 0
	global_load_dwordx4 v[48:51], v[50:51], off nt
	v_lshl_add_u64 v[62:63], v[62:63], 0, v[128:129]
	global_load_dwordx4 v[68:71], v[60:61], off nt
	global_load_dwordx4 v[64:67], v[62:63], off nt
	v_readlane_b32 s40, v254, 2
	v_and_b32_e32 v56, 7, v56
	v_readlane_b32 s42, v254, 4
	v_lshlrev_b32_e32 v130, 4, v56
	v_mul_u32_u24_e32 v56, 0x840, v56
	v_lshlrev_b32_e32 v60, 2, v132
	v_readlane_b32 s43, v254, 5
	s_add_u32 s13, s42, 0x12400000
	v_add_u32_e32 v57, s33, v130
	s_movk_i32 s2, 0x84
	v_add3_u32 v148, s33, v56, v60
	s_addc_u32 s33, s43, 0
	v_mul_lo_u32 v59, v132, s2
	s_add_u32 s34, s42, 0x2400000
	s_mov_b32 s15, 0
	s_mov_b32 s14, 8
	v_mov_b32_e32 v131, v129
	s_addc_u32 s35, s43, 0
	v_lshlrev_b32_e32 v128, 2, v58
	v_add_u32_e32 v149, v57, v59
	s_movk_i32 s42, 0x7f
	v_readlane_b32 s41, v254, 3
	s_waitcnt vmcnt(0)
	s_branch .LBB0_371

; #define LAS __attribute__((address_space(3)))
; DI void cv_finish(const CvItem& cc, int lane, LAS float* scr, const f32x4 (&v)[16]) {
;     { const int c4 = (lane & 7) * 4, r8 = lane >> 3;
; #pragma unroll
;       for (int i = 0; i < 16; ++i) { LAS float* d = scr + (8 * i + r8) * 33 + c4; d[0] = v[i][0]; d[1] = v[i][1]; d[2] = v[i][2]; d[3] = v[i][3]; } }
; DI void conv_pool(const Params& P, LAS unsigned char* lds, int pool, int blk_lo, int blk_hi) {
;     ...
;     for (;;) { int nx = it + 1; bool more = true;
;     ...
;         const CvItem nxt = cv_decode(P, nx); f32x4 vn[16]; cv_issue(nxt, lane, vn);
.LBB0_370:
	s_lshr_b32 s39, s48, 5
	s_sext_i32_i16 s2, s38
	v_cvt_f32_ubyte0_e32 v57, s39
	v_cvt_f32_i32_e32 v56, s2
	v_rcp_iflag_f32_e32 v58, v57
	s_ashr_i32 s2, s2, 30
	s_or_b32 s45, s2, 1
	v_mul_f32_e32 v58, v56, v58
	v_trunc_f32_e32 v58, v58
	v_fma_f32 v56, -v58, v57, v56
	v_cvt_i32_f32_e32 v58, v58
	v_cmp_ge_f32_e64 s[2:3], |v56|, v57
	s_and_b64 s[2:3], s[2:3], exec
	s_cselect_b32 s2, s45, 0
	v_readfirstlane_b32 s3, v58
	s_add_i32 s2, s3, s2
	s_sext_i32_i16 s3, s2
	s_mul_i32 s2, s2, s39
	s_sub_i32 s2, s38, s2
	s_sext_i32_i16 s2, s2
	s_lshl_b32 s45, s3, 7
	s_lshl_b32 s38, s2, 5
	v_add_u32_e32 v56, s45, v132
	v_add_u32_e32 v58, s45, v133
	s_waitcnt vmcnt(19)
	v_add_u32_e32 v72, s45, v134
	v_add_u32_e32 v74, s45, v135
	v_add_u32_e32 v80, s45, v136
	v_add_u32_e32 v82, s45, v137
	v_add_u32_e32 v88, s45, v138
	v_add_u32_e32 v90, s45, v139
	v_add_u32_e32 v96, s45, v140
	v_add_u32_e32 v98, s45, v141
	v_add_u32_e32 v104, s45, v142
	v_add_u32_e32 v106, s45, v143
	v_add_u32_e32 v112, s45, v144
	v_add_u32_e32 v114, s45, v145
	v_add_u32_e32 v120, s45, v146
	v_add_u32_e32 v122, s45, v147
	v_mad_i64_i32 v[56:57], s[2:3], v56, s48, 0
	s_ashr_i32 s39, s38, 31
	v_mad_i64_i32 v[58:59], s[50:51], v58, s48, 0
	v_mad_i64_i32 v[72:73], s[50:51], v72, s48, 0
	v_mad_i64_i32 v[74:75], s[50:51], v74, s48, 0
	v_mad_i64_i32 v[80:81], s[50:51], v80, s48, 0
	v_mad_i64_i32 v[82:83], s[50:51], v82, s48, 0
	v_mad_i64_i32 v[88:89], s[50:51], v88, s48, 0
	v_mad_i64_i32 v[90:91], s[50:51], v90, s48, 0
	v_mad_i64_i32 v[96:97], s[50:51], v96, s48, 0
	v_mad_i64_i32 v[98:99], s[50:51], v98, s48, 0
	v_mad_i64_i32 v[104:105], s[50:51], v104, s48, 0
	v_mad_i64_i32 v[106:107], s[50:51], v106, s48, 0
	v_mad_i64_i32 v[112:113], s[50:51], v112, s48, 0
	v_mad_i64_i32 v[114:115], s[50:51], v114, s48, 0
	v_mad_i64_i32 v[120:121], s[50:51], v120, s48, 0
	v_mad_i64_i32 v[122:123], s[48:49], v122, s48, 0
	v_lshl_add_u64 v[56:57], v[56:57], 2, s[40:41]
	s_lshl_b64 s[2:3], s[38:39], 2
	v_lshl_add_u64 v[58:59], v[58:59], 2, s[40:41]
	v_lshl_add_u64 v[72:73], v[72:73], 2, s[40:41]
	v_lshl_add_u64 v[74:75], v[74:75], 2, s[40:41]
	v_lshl_add_u64 v[80:81], v[80:81], 2, s[40:41]
	v_lshl_add_u64 v[82:83], v[82:83], 2, s[40:41]
	v_lshl_add_u64 v[88:89], v[88:89], 2, s[40:41]
	v_lshl_add_u64 v[90:91], v[90:91], 2, s[40:41]
	v_lshl_add_u64 v[96:97], v[96:97], 2, s[40:41]
	v_lshl_add_u64 v[98:99], v[98:99], 2, s[40:41]
	v_lshl_add_u64 v[104:105], v[104:105], 2, s[40:41]
	v_lshl_add_u64 v[106:107], v[106:107], 2, s[40:41]
	v_lshl_add_u64 v[112:113], v[112:113], 2, s[40:41]
	v_lshl_add_u64 v[114:115], v[114:115], 2, s[40:41]
	v_lshl_add_u64 v[120:121], v[120:121], 2, s[40:41]
	v_lshl_add_u64 v[122:123], v[122:123], 2, s[40:41]
	v_lshl_add_u64 v[56:57], v[56:57], 0, s[2:3]
	v_lshl_add_u64 v[58:59], v[58:59], 0, s[2:3]
	v_lshl_add_u64 v[72:73], v[72:73], 0, s[2:3]
	v_lshl_add_u64 v[74:75], v[74:75], 0, s[2:3]
	v_lshl_add_u64 v[80:81], v[80:81], 0, s[2:3]
	v_lshl_add_u64 v[82:83], v[82:83], 0, s[2:3]
	v_lshl_add_u64 v[88:89], v[88:89], 0, s[2:3]
	v_lshl_add_u64 v[90:91], v[90:91], 0, s[2:3]
	v_lshl_add_u64 v[96:97], v[96:97], 0, s[2:3]
	v_lshl_add_u64 v[98:99], v[98:99], 0, s[2:3]
	v_lshl_add_u64 v[104:105], v[104:105], 0, s[2:3]
	v_lshl_add_u64 v[106:107], v[106:107], 0, s[2:3]
	v_lshl_add_u64 v[112:113], v[112:113], 0, s[2:3]
	v_lshl_add_u64 v[114:115], v[114:115], 0, s[2:3]
	v_lshl_add_u64 v[120:121], v[120:121], 0, s[2:3]
	v_lshl_add_u64 v[122:123], v[122:123], 0, s[2:3]
	v_lshl_add_u64 v[56:57], v[56:57], 0, v[128:129]
	v_lshl_add_u64 v[60:61], v[58:59], 0, v[128:129]
	v_lshl_add_u64 v[72:73], v[72:73], 0, v[128:129]
	s_waitcnt vmcnt(17)
	v_lshl_add_u64 v[76:77], v[74:75], 0, v[128:129]
	v_lshl_add_u64 v[80:81], v[80:81], 0, v[128:129]
	v_lshl_add_u64 v[84:85], v[82:83], 0, v[128:129]
	v_lshl_add_u64 v[88:89], v[88:89], 0, v[128:129]
	v_lshl_add_u64 v[92:93], v[90:91], 0, v[128:129]
	v_lshl_add_u64 v[96:97], v[96:97], 0, v[128:129]
	v_lshl_add_u64 v[100:101], v[98:99], 0, v[128:129]
	v_lshl_add_u64 v[104:105], v[104:105], 0, v[128:129]
	v_lshl_add_u64 v[108:109], v[106:107], 0, v[128:129]
	v_lshl_add_u64 v[112:113], v[112:113], 0, v[128:129]
	v_lshl_add_u64 v[116:117], v[114:115], 0, v[128:129]
	v_lshl_add_u64 v[120:121], v[120:121], 0, v[128:129]
	v_lshl_add_u64 v[124:125], v[122:123], 0, v[128:129]
	global_load_dwordx4 v[56:59], v[56:57], off nt
	s_nop 0
	global_load_dwordx4 v[60:63], v[60:61], off nt
	s_nop 0
	global_load_dwordx4 v[72:75], v[72:73], off nt
	s_nop 0
	global_load_dwordx4 v[76:79], v[76:77], off nt
	s_nop 0
	global_load_dwordx4 v[80:83], v[80:81], off nt
	s_nop 0
	global_load_dwordx4 v[84:87], v[84:85], off nt
	s_nop 0
	global_load_dwordx4 v[88:91], v[88:89], off nt
	s_nop 0
	global_load_dwordx4 v[92:95], v[92:93], off nt
	s_nop 0
	global_load_dwordx4 v[96:99], v[96:97], off nt
	s_nop 0
	global_load_dwordx4 v[100:103], v[100:101], off nt
	s_nop 0
	global_load_dwordx4 v[104:107], v[104:105], off nt
	s_nop 0
	global_load_dwordx4 v[108:111], v[108:109], off nt
	s_nop 0
	global_load_dwordx4 v[112:115], v[112:113], off nt
	s_nop 0
	global_load_dwordx4 v[116:119], v[116:117], off nt
	s_nop 0
	global_load_dwordx4 v[120:123], v[120:121], off nt
	s_nop 0
	global_load_dwordx4 v[124:127], v[124:125], off nt
	ds_write2_b32 v149, v4, v5 offset1:1
	ds_write2_b32 v149, v6, v7 offset0:2 offset1:3
	v_add_u32_e32 v4, 0x420, v149
	ds_write2_b32 v4, v0, v1 offset1:1
	v_add_u32_e32 v0, 0x428, v149
	ds_write2_b32 v0, v2, v3 offset1:1
	v_add_u32_e32 v0, 0x840, v149
	ds_write2_b32 v0, v12, v13 offset1:1
	v_add_u32_e32 v0, 0x848, v149
	ds_write2_b32 v0, v14, v15 offset1:1
	v_add_u32_e32 v0, 0xc60, v149
; #define LAS __attribute__((address_space(3)))
; DI unsigned pk4f8(float a, float b, float c, float d) { int p = __builtin_amdgcn_cvt_pk_fp8_f32(a, b, 0, false); p = __builtin_amdgcn_cvt_pk_fp8_f32(c, d, p, true); return (unsigned)p; }
; DI void cv_finish(const CvItem& cc, int lane, LAS float* scr, const f32x4 (&v)[16]) {
;     { const int c4 = (lane & 7) * 4, r8 = lane >> 3;
; #pragma unroll
;       for (int i = 0; i < 16; ++i) { LAS float* d = scr + (8 * i + r8) * 33 + c4; d[0] = v[i][0]; d[1] = v[i][1]; d[2] = v[i][2]; d[3] = v[i][3]; } }
;     asm volatile("s_waitcnt lgkmcnt(0)" ::: "memory");
;     const int c = lane & 7;
; #pragma unroll
;     for (int j = 0; j < 4; ++j) { const int n = (lane >> 3) + 8 * j; const int src = cc.n0 + n; int dst = src;
;         if (cc.kind == 2) { const int jj = src & 2047; dst = (jj >> 7) * 256 + (src >> 11) * 128 + (jj & 127); }
;         const LAS float* sp = scr + (16 * c) * 33 + n;
;         u32x4 o; o.x = pk4f8(sp[0 * 33] * WSCALE, sp[1 * 33] * WSCALE, sp[2 * 33] * WSCALE, sp[3 * 33] * WSCALE); o.y = pk4f8(sp[4 * 33] * WSCALE, sp[5 * 33] * WSCALE, sp[6 * 33] * WSCALE, sp[7 * 33] * WSCALE);
;         o.z = pk4f8(sp[8 * 33] * WSCALE, sp[9 * 33] * WSCALE, sp[10 * 33] * WSCALE, sp[11 * 33] * WSCALE); o.w = pk4f8(sp[12 * 33] * WSCALE, sp[13 * 33] * WSCALE, sp[14 * 33] * WSCALE, sp[15 * 33] * WSCALE);
;         *(u32x4*)(cc.WT + (size_t)dst * D + cc.k0 + 16 * c) = o; }
	ds_write2_b32 v0, v8, v9 offset1:1
	v_add_u32_e32 v0, 0xc68, v149
	ds_write2_b32 v0, v10, v11 offset1:1
	v_add_u32_e32 v0, 0x1080, v149
	ds_write2_b32 v0, v20, v21 offset1:1
	v_add_u32_e32 v0, 0x1088, v149
	ds_write2_b32 v0, v22, v23 offset1:1
	v_add_u32_e32 v0, 0x14a0, v149
	ds_write2_b32 v0, v16, v17 offset1:1
	v_add_u32_e32 v0, 0x14a8, v149
	ds_write2_b32 v0, v18, v19 offset1:1
	v_add_u32_e32 v0, 0x18c0, v149
	ds_write2_b32 v0, v28, v29 offset1:1
	v_add_u32_e32 v0, 0x18c8, v149
	ds_write2_b32 v0, v30, v31 offset1:1
	v_add_u32_e32 v0, 0x1ce0, v149
	ds_write2_b32 v0, v24, v25 offset1:1
	v_add_u32_e32 v0, 0x1ce8, v149
	ds_write2_b32 v0, v26, v27 offset1:1
	v_add_u32_e32 v0, 0x2100, v149
	ds_write2_b32 v0, v36, v37 offset1:1
	v_add_u32_e32 v0, 0x2108, v149
	ds_write2_b32 v0, v38, v39 offset1:1
	v_add_u32_e32 v0, 0x2520, v149
	ds_write2_b32 v0, v32, v33 offset1:1
	v_add_u32_e32 v0, 0x2528, v149
	ds_write2_b32 v0, v34, v35 offset1:1
	v_add_u32_e32 v0, 0x2940, v149
	ds_write2_b32 v0, v44, v45 offset1:1
	v_add_u32_e32 v0, 0x2948, v149
	ds_write2_b32 v0, v46, v47 offset1:1
	v_add_u32_e32 v0, 0x2d60, v149
	ds_write2_b32 v0, v40, v41 offset1:1
	v_add_u32_e32 v0, 0x2d68, v149
	ds_write2_b32 v0, v42, v43 offset1:1
	v_add_u32_e32 v0, 0x3180, v149
	ds_write2_b32 v0, v52, v53 offset1:1
	v_add_u32_e32 v0, 0x3188, v149
	ds_write2_b32 v0, v54, v55 offset1:1
	v_add_u32_e32 v0, 0x35a0, v149
	ds_write2_b32 v0, v48, v49 offset1:1
	v_add_u32_e32 v0, 0x35a8, v149
	ds_write2_b32 v0, v50, v51 offset1:1
	v_add_u32_e32 v0, 0x39c0, v149
	ds_write2_b32 v0, v68, v69 offset1:1
	v_add_u32_e32 v0, 0x39c8, v149
	ds_write2_b32 v0, v70, v71 offset1:1
	v_add_u32_e32 v0, 0x3de0, v149
	ds_write2_b32 v0, v64, v65 offset1:1
	v_add_u32_e32 v0, 0x3de8, v149
	ds_write2_b32 v0, v66, v67 offset1:1
	s_waitcnt lgkmcnt(0)
	v_add_u32_e32 v0, s12, v132
	v_lshlrev_b32_e32 v1, 1, v0
	v_ashrrev_i32_e32 v2, 4, v0
	ds_read2_b32 v[4:5], v148 offset1:8
	ds_read2_b32 v[6:7], v148 offset0:33 offset1:41
	ds_read2_b32 v[8:9], v148 offset0:66 offset1:74
	v_and_b32_e32 v1, 0xf00, v1
	v_and_b32_e32 v2, 0xffffff80, v2
	s_cmp_eq_u32 s11, 2
	v_add_u32_e32 v1, v1, v2
	v_and_or_b32 v1, v0, s42, v1
	s_cselect_b64 vcc, -1, 0
	ds_read2_b32 v[12:13], v148 offset0:99 offset1:107
	v_cndmask_b32_e32 v10, v0, v1, vcc
	s_waitcnt lgkmcnt(3)
	v_mul_f32_e32 v1, 0x44000000, v4
	s_waitcnt lgkmcnt(2)
	v_mul_f32_e32 v2, 0x44000000, v6
	v_mov_b32_e32 v0, v129
	v_cvt_pk_fp8_f32 v0, v1, v2
	ds_read2_b32 v[14:15], v148 offset0:132 offset1:140
	ds_read2_b32 v[16:17], v148 offset0:165 offset1:173
	ds_read2_b32 v[18:19], v148 offset0:198 offset1:206
	s_waitcnt lgkmcnt(4)
	v_mul_f32_e32 v3, 0x44000000, v8
	s_waitcnt lgkmcnt(3)
	v_mul_f32_e32 v1, 0x44000000, v12
	ds_read2_b32 v[20:21], v148 offset0:231 offset1:239
	v_add_u32_e32 v38, 0x400, v148
	v_cvt_pk_fp8_f32 v0, v3, v1 op_sel:[0,0,1]
	s_waitcnt lgkmcnt(3)
	v_mul_f32_e32 v2, 0x44000000, v14
	s_waitcnt lgkmcnt(2)
	v_mul_f32_e32 v3, 0x44000000, v16
	v_mov_b32_e32 v1, v129
	ds_read2_b32 v[22:23], v38 offset0:8 offset1:16
	v_cvt_pk_fp8_f32 v1, v2, v3
	ds_read2_b32 v[24:25], v38 offset0:41 offset1:49
	ds_read2_b32 v[26:27], v38 offset0:74 offset1:82
	ds_read2_b32 v[28:29], v38 offset0:107 offset1:115
	ds_read2_b32 v[30:31], v38 offset0:140 offset1:148
	ds_read2_b32 v[32:33], v38 offset0:173 offset1:181
	s_waitcnt lgkmcnt(7)
	v_mul_f32_e32 v4, 0x44000000, v18
	s_waitcnt lgkmcnt(6)
	v_mul_f32_e32 v2, 0x44000000, v20
	v_cvt_pk_fp8_f32 v1, v4, v2 op_sel:[0,0,1]
	s_waitcnt lgkmcnt(5)
	v_mul_f32_e32 v3, 0x44000000, v22
	s_waitcnt lgkmcnt(4)
	v_mul_f32_e32 v4, 0x44000000, v24
	v_mov_b32_e32 v2, v129
	ds_read2_b32 v[34:35], v38 offset0:206 offset1:214
	ds_read2_b32 v[36:37], v38 offset0:239 offset1:247
	v_cvt_pk_fp8_f32 v2, v3, v4
	s_waitcnt lgkmcnt(3)
	v_mul_f32_e32 v4, 0x44000000, v30
	s_waitcnt lgkmcnt(2)
	v_mul_f32_e32 v11, 0x44000000, v32
	v_mov_b32_e32 v3, v129
	v_cvt_pk_fp8_f32 v3, v4, v11
	v_mul_f32_e32 v6, 0x44000000, v26
	v_mul_f32_e32 v8, 0x44000000, v28
	v_cvt_pk_fp8_f32 v2, v6, v8 op_sel:[0,0,1]
	s_waitcnt lgkmcnt(1)
	v_mul_f32_e32 v4, 0x44000000, v34
	s_waitcnt lgkmcnt(0)
	v_mul_f32_e32 v6, 0x44000000, v36
	v_ashrrev_i32_e32 v11, 31, v10
	v_cvt_pk_fp8_f32 v3, v4, v6 op_sel:[0,0,1]
	v_lshlrev_b64 v[10:11], 11, v[10:11]
	v_lshl_add_u64 v[10:11], s[6:7], 0, v[10:11]
	s_ashr_i32 s11, s10, 31
	v_lshl_add_u64 v[10:11], v[10:11], 0, s[10:11]
	v_lshl_add_u64 v[10:11], v[10:11], 0, v[130:131]
	global_store_dwordx4 v[10:11], v[0:3], off
	v_mul_f32_e32 v6, 0x44000000, v17
	v_mul_f32_e32 v8, 0x44000000, v33
	v_add_u32_e32 v0, s12, v133
	v_lshlrev_b32_e32 v1, 1, v0
	v_ashrrev_i32_e32 v2, 4, v0
	v_and_b32_e32 v1, 0xf00, v1
	v_and_b32_e32 v2, 0xffffff80, v2
	v_add_u32_e32 v1, v1, v2
	v_and_or_b32 v1, v0, s42, v1
	v_cndmask_b32_e32 v4, v0, v1, vcc
	v_mul_f32_e32 v1, 0x44000000, v5
	v_mul_f32_e32 v2, 0x44000000, v7
	v_mov_b32_e32 v0, v129
	v_cvt_pk_fp8_f32 v0, v1, v2
	v_mul_f32_e32 v2, 0x44000000, v15
	v_mov_b32_e32 v1, v129
	v_cvt_pk_fp8_f32 v1, v2, v6
	v_mul_f32_e32 v3, 0x44000000, v9
	v_mul_f32_e32 v5, 0x44000000, v13
	v_cvt_pk_fp8_f32 v0, v3, v5 op_sel:[0,0,1]
	v_mul_f32_e32 v2, 0x44000000, v19
	v_mul_f32_e32 v3, 0x44000000, v21
	v_cvt_pk_fp8_f32 v1, v2, v3 op_sel:[0,0,1]
	v_mul_f32_e32 v3, 0x44000000, v23
	v_mul_f32_e32 v5, 0x44000000, v25
	v_mov_b32_e32 v2, v129
	v_cvt_pk_fp8_f32 v2, v3, v5
	v_mul_f32_e32 v5, 0x44000000, v31
	v_mov_b32_e32 v3, v129
	v_cvt_pk_fp8_f32 v3, v5, v8
	v_mul_f32_e32 v6, 0x44000000, v27
	v_mul_f32_e32 v7, 0x44000000, v29
	v_cvt_pk_fp8_f32 v2, v6, v7 op_sel:[0,0,1]
	v_mul_f32_e32 v5, 0x44000000, v35
	v_mul_f32_e32 v6, 0x44000000, v37
	v_cvt_pk_fp8_f32 v3, v5, v6 op_sel:[0,0,1]
	v_ashrrev_i32_e32 v5, 31, v4
	v_lshlrev_b64 v[4:5], 11, v[4:5]
	v_lshl_add_u64 v[4:5], s[6:7], 0, v[4:5]
	v_lshl_add_u64 v[4:5], v[4:5], 0, s[10:11]
	v_lshl_add_u64 v[4:5], v[4:5], 0, v[130:131]
	global_store_dwordx4 v[4:5], v[0:3], off
	ds_read2_b32 v[4:5], v148 offset0:16 offset1:24
	ds_read2_b32 v[6:7], v148 offset0:49 offset1:57
	ds_read2_b32 v[8:9], v148 offset0:82 offset1:90
	v_add_u32_e32 v0, s12, v134
	v_lshlrev_b32_e32 v1, 1, v0
	v_ashrrev_i32_e32 v2, 4, v0
	v_and_b32_e32 v1, 0xf00, v1
	v_and_b32_e32 v2, 0xffffff80, v2
	v_add_u32_e32 v1, v1, v2
	v_and_or_b32 v1, v0, s42, v1
	ds_read2_b32 v[12:13], v148 offset0:115 offset1:123
	v_cndmask_b32_e32 v10, v0, v1, vcc
	s_waitcnt lgkmcnt(3)
; #define LAS __attribute__((address_space(3)))
; DI unsigned pk4f8(float a, float b, float c, float d) { int p = __builtin_amdgcn_cvt_pk_fp8_f32(a, b, 0, false); p = __builtin_amdgcn_cvt_pk_fp8_f32(c, d, p, true); return (unsigned)p; }
; DI void cv_finish(const CvItem& cc, int lane, LAS float* scr, const f32x4 (&v)[16]) {
;     ...
; #pragma unroll
;     for (int j = 0; j < 4; ++j) { const int n = (lane >> 3) + 8 * j; const int src = cc.n0 + n; int dst = src;
;         if (cc.kind == 2) { const int jj = src & 2047; dst = (jj >> 7) * 256 + (src >> 11) * 128 + (jj & 127); }
;         const LAS float* sp = scr + (16 * c) * 33 + n;
;         u32x4 o; o.x = pk4f8(sp[0 * 33] * WSCALE, sp[1 * 33] * WSCALE, sp[2 * 33] * WSCALE, sp[3 * 33] * WSCALE); o.y = pk4f8(sp[4 * 33] * WSCALE, sp[5 * 33] * WSCALE, sp[6 * 33] * WSCALE, sp[7 * 33] * WSCALE);
;         o.z = pk4f8(sp[8 * 33] * WSCALE, sp[9 * 33] * WSCALE, sp[10 * 33] * WSCALE, sp[11 * 33] * WSCALE); o.w = pk4f8(sp[12 * 33] * WSCALE, sp[13 * 33] * WSCALE, sp[14 * 33] * WSCALE, sp[15 * 33] * WSCALE);
;         *(u32x4*)(cc.WT + (size_t)dst * D + cc.k0 + 16 * c) = o; }
;     asm volatile("s_waitcnt lgkmcnt(0)" ::: "memory");
; DI void conv_pool(const Params& P, LAS unsigned char* lds, int pool, int blk_lo, int blk_hi) {
;     ...
;         cv_finish(cur, lane, scr, v);
;         if (!more) break;
; #pragma unroll
;         for (int i = 0; i < 16; ++i) v[i] = vn[i];
;         cur = nxt; it = nx; }
	v_mul_f32_e32 v1, 0x44000000, v4
	s_waitcnt lgkmcnt(2)
	v_mul_f32_e32 v2, 0x44000000, v6
	v_mov_b32_e32 v0, v129
	ds_read2_b32 v[14:15], v148 offset0:148 offset1:156
	ds_read2_b32 v[16:17], v148 offset0:181 offset1:189
	v_cvt_pk_fp8_f32 v0, v1, v2
	s_waitcnt lgkmcnt(3)
	v_mul_f32_e32 v3, 0x44000000, v8
	s_waitcnt lgkmcnt(2)
	v_mul_f32_e32 v1, 0x44000000, v12
	ds_read2_b32 v[18:19], v148 offset0:214 offset1:222
	ds_read2_b32 v[20:21], v148 offset0:247 offset1:255
	v_cvt_pk_fp8_f32 v0, v3, v1 op_sel:[0,0,1]
	s_waitcnt lgkmcnt(3)
	v_mul_f32_e32 v2, 0x44000000, v14
	s_waitcnt lgkmcnt(2)
	v_mul_f32_e32 v3, 0x44000000, v16
	v_mov_b32_e32 v1, v129
	ds_read2_b32 v[22:23], v38 offset0:24 offset1:32
	v_cvt_pk_fp8_f32 v1, v2, v3
	ds_read2_b32 v[24:25], v38 offset0:57 offset1:65
	ds_read2_b32 v[26:27], v38 offset0:90 offset1:98
	ds_read2_b32 v[28:29], v38 offset0:123 offset1:131
	ds_read2_b32 v[30:31], v38 offset0:156 offset1:164
	ds_read2_b32 v[32:33], v38 offset0:189 offset1:197
	s_waitcnt lgkmcnt(7)
	v_mul_f32_e32 v4, 0x44000000, v18
	s_waitcnt lgkmcnt(6)
	v_mul_f32_e32 v2, 0x44000000, v20
	v_cvt_pk_fp8_f32 v1, v4, v2 op_sel:[0,0,1]
	s_waitcnt lgkmcnt(5)
	v_mul_f32_e32 v3, 0x44000000, v22
	s_waitcnt lgkmcnt(4)
	v_mul_f32_e32 v4, 0x44000000, v24
	v_mov_b32_e32 v2, v129
	v_cvt_pk_fp8_f32 v2, v3, v4
	v_add_u32_e32 v3, 0x600, v148
	ds_read2_b32 v[34:35], v38 offset0:222 offset1:230
	ds_read2_b32 v[36:37], v3 offset0:127 offset1:135
	s_waitcnt lgkmcnt(3)
	v_mul_f32_e32 v4, 0x44000000, v30
	s_waitcnt lgkmcnt(2)
	v_mul_f32_e32 v11, 0x44000000, v32
	v_mov_b32_e32 v3, v129
	v_cvt_pk_fp8_f32 v3, v4, v11
	v_mul_f32_e32 v6, 0x44000000, v26
	v_mul_f32_e32 v8, 0x44000000, v28
	v_cvt_pk_fp8_f32 v2, v6, v8 op_sel:[0,0,1]
	s_waitcnt lgkmcnt(1)
	v_mul_f32_e32 v4, 0x44000000, v34
	s_waitcnt lgkmcnt(0)
	v_mul_f32_e32 v6, 0x44000000, v36
	v_ashrrev_i32_e32 v11, 31, v10
	v_cvt_pk_fp8_f32 v3, v4, v6 op_sel:[0,0,1]
	v_lshlrev_b64 v[10:11], 11, v[10:11]
	v_lshl_add_u64 v[10:11], s[6:7], 0, v[10:11]
	v_lshl_add_u64 v[10:11], v[10:11], 0, s[10:11]
	v_lshl_add_u64 v[10:11], v[10:11], 0, v[130:131]
	global_store_dwordx4 v[10:11], v[0:3], off
	v_mul_f32_e32 v6, 0x44000000, v17
	v_mul_f32_e32 v8, 0x44000000, v33
	v_add_u32_e32 v0, s12, v135
	v_lshlrev_b32_e32 v1, 1, v0
	v_ashrrev_i32_e32 v2, 4, v0
	v_and_b32_e32 v1, 0xf00, v1
	v_and_b32_e32 v2, 0xffffff80, v2
	v_add_u32_e32 v1, v1, v2
	v_and_or_b32 v1, v0, s42, v1
	v_cndmask_b32_e32 v4, v0, v1, vcc
	v_mul_f32_e32 v1, 0x44000000, v5
	v_mul_f32_e32 v2, 0x44000000, v7
	v_mov_b32_e32 v0, v129
	v_cvt_pk_fp8_f32 v0, v1, v2
	v_mul_f32_e32 v2, 0x44000000, v15
	v_mov_b32_e32 v1, v129
	v_cvt_pk_fp8_f32 v1, v2, v6
	v_mul_f32_e32 v3, 0x44000000, v9
	v_mul_f32_e32 v5, 0x44000000, v13
	v_cvt_pk_fp8_f32 v0, v3, v5 op_sel:[0,0,1]
	v_mul_f32_e32 v2, 0x44000000, v19
	v_mul_f32_e32 v3, 0x44000000, v21
	v_cvt_pk_fp8_f32 v1, v2, v3 op_sel:[0,0,1]
	v_mul_f32_e32 v3, 0x44000000, v23
	v_mul_f32_e32 v5, 0x44000000, v25
	v_mov_b32_e32 v2, v129
	v_cvt_pk_fp8_f32 v2, v3, v5
	v_mul_f32_e32 v5, 0x44000000, v31
	v_mov_b32_e32 v3, v129
	v_cvt_pk_fp8_f32 v3, v5, v8
	v_mul_f32_e32 v6, 0x44000000, v27
	v_mul_f32_e32 v7, 0x44000000, v29
	v_cvt_pk_fp8_f32 v2, v6, v7 op_sel:[0,0,1]
	v_mul_f32_e32 v5, 0x44000000, v35
	v_mul_f32_e32 v6, 0x44000000, v37
	v_cvt_pk_fp8_f32 v3, v5, v6 op_sel:[0,0,1]
	v_ashrrev_i32_e32 v5, 31, v4
	v_lshlrev_b64 v[4:5], 11, v[4:5]
	v_lshl_add_u64 v[4:5], s[6:7], 0, v[4:5]
	v_lshl_add_u64 v[4:5], v[4:5], 0, s[10:11]
	v_lshl_add_u64 v[4:5], v[4:5], 0, v[130:131]
	global_store_dwordx4 v[4:5], v[0:3], off
	s_waitcnt lgkmcnt(0)
	s_waitcnt vmcnt(19)
	v_mov_b64_e32 v[4:5], v[56:57]
	s_waitcnt vmcnt(17)
	v_mov_b64_e32 v[12:13], v[72:73]
	v_mov_b64_e32 v[0:1], v[60:61]
	s_waitcnt vmcnt(16)
	v_mov_b64_e32 v[8:9], v[76:77]
	s_waitcnt vmcnt(15)
	v_mov_b64_e32 v[20:21], v[80:81]
	s_waitcnt vmcnt(14)
	v_mov_b64_e32 v[16:17], v[84:85]
	s_waitcnt vmcnt(13)
	v_mov_b64_e32 v[28:29], v[88:89]
	s_waitcnt vmcnt(12)
	v_mov_b64_e32 v[24:25], v[92:93]
	s_waitcnt vmcnt(11)
	v_mov_b64_e32 v[36:37], v[96:97]
	s_waitcnt vmcnt(10)
	v_mov_b64_e32 v[32:33], v[100:101]
	s_waitcnt vmcnt(9)
	v_mov_b64_e32 v[44:45], v[104:105]
	s_waitcnt vmcnt(8)
	v_mov_b64_e32 v[40:41], v[108:109]
	s_waitcnt vmcnt(7)
	v_mov_b64_e32 v[52:53], v[112:113]
	s_waitcnt vmcnt(6)
	v_mov_b64_e32 v[48:49], v[116:117]
	s_waitcnt vmcnt(5)
	v_mov_b64_e32 v[68:69], v[120:121]
	s_waitcnt vmcnt(4)
	v_mov_b64_e32 v[64:65], v[124:125]
	s_andn2_b64 vcc, exec, s[22:23]
	v_mov_b64_e32 v[6:7], v[58:59]
	v_mov_b64_e32 v[2:3], v[62:63]
	v_mov_b64_e32 v[14:15], v[74:75]
	v_mov_b64_e32 v[10:11], v[78:79]
	v_mov_b64_e32 v[22:23], v[82:83]
	v_mov_b64_e32 v[18:19], v[86:87]
	v_mov_b64_e32 v[30:31], v[90:91]
	v_mov_b64_e32 v[26:27], v[94:95]
	v_mov_b64_e32 v[38:39], v[98:99]
	v_mov_b64_e32 v[34:35], v[102:103]
	v_mov_b64_e32 v[46:47], v[106:107]
	v_mov_b64_e32 v[42:43], v[110:111]
	v_mov_b64_e32 v[54:55], v[114:115]
	v_mov_b64_e32 v[50:51], v[118:119]
	v_mov_b64_e32 v[70:71], v[122:123]
	v_mov_b64_e32 v[66:67], v[126:127]
	s_mov_b64 s[6:7], s[16:17]
	s_mov_b32 s11, s14
	s_mov_b32 s10, s45
	s_mov_b32 s12, s38
	s_mov_b32 s38, s44
	s_mov_b32 s14, s43
	s_cbranch_vccz .LBB0_383

; DI CvItem cv_decode(const Params& P, int it) { CvItem c; int item;
;     if (it < NE * CV_GU1) { const int e = it / CV_GU1; c.W = P.in[I_WGU] + (size_t)e * D * 4096; c.N = 4096; c.WT = (unsigned char*)(P.ws + WS_WGU) + (size_t)e * 4096 * D; c.kind = 2; item = it % CV_GU1; }
;     else { const int r = it - NE * CV_GU1; const int e = r / CV_DN1; c.W = P.in[I_WDN] + (size_t)e * D * D; c.N = D; c.WT = (unsigned char*)(P.ws + WS_WDN) + (size_t)e * D * D; c.kind = 3; item = r % CV_DN1; }
;     const int nblk = c.N / 32, kb = item / nblk, nb = item % nblk; c.k0 = 128 * kb; c.n0 = 32 * nb; return c; }
; DI void cv_issue(const CvItem& c, int lane, f32x4 (&v)[16]) { const int c4 = (lane & 7) * 4, r8 = lane >> 3;
; #pragma unroll
;     for (int i = 0; i < 16; ++i) v[i] = *(const f32x4*)(c.W + (size_t)(c.k0 + 8 * i + r8) * c.N + c.n0 + c4); }
; DI void conv_pool(const Params& P, LAS unsigned char* lds, int pool, int blk_lo, int blk_hi) {
;     ...
;     auto claim = [&]() -> int { unsigned v_ = 0u; if (lane == 0) v_ = __hip_atomic_fetch_add(ctr, 1u, __ATOMIC_RELAXED, __HIP_MEMORY_SCOPE_AGENT); return blk_lo + (int)__builtin_amdgcn_readfirstlane(v_); };
;     const int blk = claim(); if (blk >= CV_NBLK) return;
;     int it = blk * CV_BLK, left = CV_BLK;
;     CvItem cur = cv_decode(P, it); f32x4 v[16]; cv_issue(cur, lane, v);
.LBB0_1121:
	s_lshr_b32 s13, s16, 5
	s_sext_i32_i16 s2, s10
	v_cvt_f32_ubyte0_e32 v1, s13
	v_cvt_f32_i32_e32 v0, s2
	v_rcp_iflag_f32_e32 v2, v1
	s_mulk_i32 s12, 0x4200
	s_ashr_i32 s2, s2, 30
	s_add_i32 s17, s12, 0
	v_mul_f32_e32 v2, v0, v2
	v_trunc_f32_e32 v2, v2
	v_fma_f32 v0, -v2, v1, v0
	v_cvt_i32_f32_e32 v2, v2
	s_or_b32 s12, s2, 1
	v_cmp_ge_f32_e64 s[2:3], |v0|, v1
	s_and_b64 s[2:3], s[2:3], exec
	s_cselect_b32 s2, s12, 0
	v_readfirstlane_b32 s3, v2
	s_add_i32 s2, s3, s2
	s_sext_i32_i16 s3, s2
	s_mul_i32 s2, s2, s13
	s_sub_i32 s2, s10, s2
	s_sext_i32_i16 s2, s2
	s_lshl_b32 s10, s3, 7
	v_lshlrev_b32_e32 v0, 2, v56
	s_waitcnt vmcnt(15)
	v_ashrrev_i32_e32 v132, 3, v56
	s_lshl_b32 s12, s2, 5
	v_and_b32_e32 v58, 28, v0
	v_add_u32_e32 v0, s10, v132
	v_mad_i64_i32 v[0:1], s[2:3], v0, s16, 0
	s_ashr_i32 s13, s12, 31
	v_lshl_add_u64 v[0:1], v[0:1], 2, s[14:15]
	s_lshl_b64 s[2:3], s[12:13], 2
	s_waitcnt vmcnt(10)
	v_mov_b32_e32 v129, 0
	v_lshl_add_u64 v[0:1], v[0:1], 0, s[2:3]
	v_lshlrev_b32_e32 v128, 2, v58
	v_add_u32_e32 v133, 8, v132
	v_lshl_add_u64 v[8:9], v[0:1], 0, v[128:129]
	v_add_u32_e32 v0, s10, v133
	v_mad_i64_i32 v[0:1], s[18:19], v0, s16, 0
	v_lshl_add_u64 v[0:1], v[0:1], 2, s[14:15]
	v_lshl_add_u64 v[0:1], v[0:1], 0, s[2:3]
	v_add_u32_e32 v134, 16, v132
	v_lshl_add_u64 v[10:11], v[0:1], 0, v[128:129]
	global_load_dwordx4 v[4:7], v[8:9], off nt
	global_load_dwordx4 v[0:3], v[10:11], off nt
	v_add_u32_e32 v8, s10, v134
	v_mad_i64_i32 v[8:9], s[18:19], v8, s16, 0
	v_lshl_add_u64 v[8:9], v[8:9], 2, s[14:15]
	v_lshl_add_u64 v[8:9], v[8:9], 0, s[2:3]
	v_add_u32_e32 v135, 24, v132
	v_lshl_add_u64 v[16:17], v[8:9], 0, v[128:129]
	v_add_u32_e32 v8, s10, v135
	v_mad_i64_i32 v[8:9], s[18:19], v8, s16, 0
	v_lshl_add_u64 v[8:9], v[8:9], 2, s[14:15]
	v_lshl_add_u64 v[8:9], v[8:9], 0, s[2:3]
	v_add_u32_e32 v136, 32, v132
	v_lshl_add_u64 v[18:19], v[8:9], 0, v[128:129]
	global_load_dwordx4 v[12:15], v[16:17], off nt
	global_load_dwordx4 v[8:11], v[18:19], off nt
	v_add_u32_e32 v16, s10, v136
	v_mad_i64_i32 v[16:17], s[18:19], v16, s16, 0
	v_lshl_add_u64 v[16:17], v[16:17], 2, s[14:15]
	v_lshl_add_u64 v[16:17], v[16:17], 0, s[2:3]
	v_add_u32_e32 v137, 40, v132
	v_lshl_add_u64 v[24:25], v[16:17], 0, v[128:129]
	v_add_u32_e32 v16, s10, v137
	v_mad_i64_i32 v[16:17], s[18:19], v16, s16, 0
	v_lshl_add_u64 v[16:17], v[16:17], 2, s[14:15]
	v_lshl_add_u64 v[16:17], v[16:17], 0, s[2:3]
	v_add_u32_e32 v138, 48, v132
	v_lshl_add_u64 v[26:27], v[16:17], 0, v[128:129]
	global_load_dwordx4 v[20:23], v[24:25], off nt
	global_load_dwordx4 v[16:19], v[26:27], off nt
	v_add_u32_e32 v24, s10, v138
	v_mad_i64_i32 v[24:25], s[18:19], v24, s16, 0
	v_lshl_add_u64 v[24:25], v[24:25], 2, s[14:15]
	v_lshl_add_u64 v[24:25], v[24:25], 0, s[2:3]
	v_add_u32_e32 v139, 56, v132
	v_lshl_add_u64 v[32:33], v[24:25], 0, v[128:129]
	v_add_u32_e32 v24, s10, v139
	v_mad_i64_i32 v[24:25], s[18:19], v24, s16, 0
	v_lshl_add_u64 v[24:25], v[24:25], 2, s[14:15]
	v_lshl_add_u64 v[24:25], v[24:25], 0, s[2:3]
	v_add_u32_e32 v140, 64, v132
	v_lshl_add_u64 v[34:35], v[24:25], 0, v[128:129]
	global_load_dwordx4 v[28:31], v[32:33], off nt
	global_load_dwordx4 v[24:27], v[34:35], off nt
	v_add_u32_e32 v32, s10, v140
	v_mad_i64_i32 v[32:33], s[18:19], v32, s16, 0
	v_lshl_add_u64 v[32:33], v[32:33], 2, s[14:15]
	v_lshl_add_u64 v[32:33], v[32:33], 0, s[2:3]
	v_add_u32_e32 v141, 0x48, v132
	v_lshl_add_u64 v[40:41], v[32:33], 0, v[128:129]
	v_add_u32_e32 v32, s10, v141
	v_mad_i64_i32 v[32:33], s[18:19], v32, s16, 0
	v_lshl_add_u64 v[32:33], v[32:33], 2, s[14:15]
	v_lshl_add_u64 v[32:33], v[32:33], 0, s[2:3]
	v_add_u32_e32 v142, 0x50, v132
	v_lshl_add_u64 v[42:43], v[32:33], 0, v[128:129]
	global_load_dwordx4 v[36:39], v[40:41], off nt
	global_load_dwordx4 v[32:35], v[42:43], off nt
	v_add_u32_e32 v40, s10, v142
	v_mad_i64_i32 v[40:41], s[18:19], v40, s16, 0
	v_lshl_add_u64 v[40:41], v[40:41], 2, s[14:15]
	v_lshl_add_u64 v[40:41], v[40:41], 0, s[2:3]
	v_add_u32_e32 v143, 0x58, v132
	v_lshl_add_u64 v[48:49], v[40:41], 0, v[128:129]
	v_add_u32_e32 v40, s10, v143
	v_mad_i64_i32 v[40:41], s[18:19], v40, s16, 0
	v_lshl_add_u64 v[40:41], v[40:41], 2, s[14:15]
	v_lshl_add_u64 v[40:41], v[40:41], 0, s[2:3]
	v_add_u32_e32 v144, 0x60, v132
	v_lshl_add_u64 v[50:51], v[40:41], 0, v[128:129]
	global_load_dwordx4 v[44:47], v[48:49], off nt
	global_load_dwordx4 v[40:43], v[50:51], off nt
	v_add_u32_e32 v48, s10, v144
	v_mad_i64_i32 v[48:49], s[18:19], v48, s16, 0
	v_lshl_add_u64 v[48:49], v[48:49], 2, s[14:15]
	v_lshl_add_u64 v[48:49], v[48:49], 0, s[2:3]
	v_add_u32_e32 v145, 0x68, v132
	s_waitcnt vmcnt(19)
	v_lshl_add_u64 v[60:61], v[48:49], 0, v[128:129]
	v_add_u32_e32 v48, s10, v145
	v_mad_i64_i32 v[48:49], s[18:19], v48, s16, 0
	v_lshl_add_u64 v[48:49], v[48:49], 2, s[14:15]
	v_add_u32_e32 v146, 0x70, v132
	v_lshl_add_u64 v[48:49], v[48:49], 0, s[2:3]
	v_add_u32_e32 v57, s10, v146
	v_add_u32_e32 v147, 0x78, v132
	v_lshl_add_u64 v[62:63], v[48:49], 0, v[128:129]
	global_load_dwordx4 v[52:55], v[60:61], off nt
	global_load_dwordx4 v[48:51], v[62:63], off nt
	v_mad_i64_i32 v[60:61], s[18:19], v57, s16, 0
	v_add_u32_e32 v57, s10, v147
	v_lshl_add_u64 v[60:61], v[60:61], 2, s[14:15]
	v_mad_i64_i32 v[62:63], s[18:19], v57, s16, 0
	v_lshl_add_u64 v[60:61], v[60:61], 0, s[2:3]
	v_lshl_add_u64 v[62:63], v[62:63], 2, s[14:15]
	v_lshl_add_u64 v[60:61], v[60:61], 0, v[128:129]
	v_lshl_add_u64 v[62:63], v[62:63], 0, s[2:3]
	v_lshl_add_u64 v[62:63], v[62:63], 0, v[128:129]
	global_load_dwordx4 v[68:71], v[60:61], off nt
	global_load_dwordx4 v[64:67], v[62:63], off nt
	v_and_b32_e32 v56, 7, v56
	v_lshlrev_b32_e32 v130, 4, v56
	v_mul_u32_u24_e32 v56, 0x840, v56
	v_lshlrev_b32_e32 v60, 2, v132
	v_add_u32_e32 v57, s17, v130
	v_add3_u32 v148, s17, v56, v60
	v_readlane_b32 s16, v254, 2
	v_readlane_b32 s18, v254, 4
	v_readlane_b32 s19, v254, 5
	s_add_u32 s13, s18, 0x12400000
	s_movk_i32 s2, 0x84
	s_addc_u32 s24, s19, 0
	v_mul_lo_u32 v59, v132, s2
	s_add_u32 s25, s18, 0x2400000
	s_mov_b32 s15, 0
	s_mov_b32 s14, 8
	v_mov_b32_e32 v131, v129
	s_addc_u32 s26, s19, 0
	v_lshlrev_b32_e32 v128, 2, v58
	v_add_u32_e32 v149, v57, v59
	s_movk_i32 s27, 0x7f
	v_readlane_b32 s17, v254, 3
	s_waitcnt vmcnt(0)
	s_branch .LBB0_1124

; #define LAS __attribute__((address_space(3)))
; DI void cv_finish(const CvItem& cc, int lane, LAS float* scr, const f32x4 (&v)[16]) {
;     { const int c4 = (lane & 7) * 4, r8 = lane >> 3;
; #pragma unroll
;       for (int i = 0; i < 16; ++i) { LAS float* d = scr + (8 * i + r8) * 33 + c4; d[0] = v[i][0]; d[1] = v[i][1]; d[2] = v[i][2]; d[3] = v[i][3]; } }
; DI void conv_pool(const Params& P, LAS unsigned char* lds, int pool, int blk_lo, int blk_hi) {
;     ...
;     for (;;) { int nx = it + 1; bool more = true;
;     ...
;         const CvItem nxt = cv_decode(P, nx); f32x4 vn[16]; cv_issue(nxt, lane, vn);
.LBB0_1123:
	s_lshr_b32 s21, s34, 5
	s_sext_i32_i16 s2, s20
	v_cvt_f32_ubyte0_e32 v57, s21
	v_cvt_f32_i32_e32 v56, s2
	v_rcp_iflag_f32_e32 v58, v57
	s_ashr_i32 s2, s2, 30
	s_or_b32 s33, s2, 1
	v_mul_f32_e32 v58, v56, v58
	v_trunc_f32_e32 v58, v58
	v_fma_f32 v56, -v58, v57, v56
	v_cvt_i32_f32_e32 v58, v58
	v_cmp_ge_f32_e64 s[2:3], |v56|, v57
	s_and_b64 s[2:3], s[2:3], exec
	s_cselect_b32 s2, s33, 0
	v_readfirstlane_b32 s3, v58
	s_add_i32 s2, s3, s2
	s_sext_i32_i16 s3, s2
	s_mul_i32 s2, s2, s21
	s_sub_i32 s2, s20, s2
	s_sext_i32_i16 s2, s2
	s_lshl_b32 s33, s3, 7
	s_lshl_b32 s20, s2, 5
	v_add_u32_e32 v56, s33, v132
	v_add_u32_e32 v58, s33, v133
	s_waitcnt vmcnt(19)
	v_add_u32_e32 v72, s33, v134
	v_add_u32_e32 v74, s33, v135
	v_add_u32_e32 v80, s33, v136
	v_add_u32_e32 v82, s33, v137
	v_add_u32_e32 v88, s33, v138
	v_add_u32_e32 v90, s33, v139
	s_waitcnt vmcnt(18)
	v_add_u32_e32 v96, s33, v140
	v_add_u32_e32 v98, s33, v141
	v_add_u32_e32 v104, s33, v142
	v_add_u32_e32 v106, s33, v143
	v_add_u32_e32 v112, s33, v144
	v_add_u32_e32 v114, s33, v145
	v_add_u32_e32 v120, s33, v146
	v_add_u32_e32 v122, s33, v147
	v_mad_i64_i32 v[56:57], s[2:3], v56, s34, 0
	s_ashr_i32 s21, s20, 31
	v_mad_i64_i32 v[58:59], s[36:37], v58, s34, 0
	v_mad_i64_i32 v[72:73], s[36:37], v72, s34, 0
	v_mad_i64_i32 v[74:75], s[36:37], v74, s34, 0
	v_mad_i64_i32 v[80:81], s[36:37], v80, s34, 0
	v_mad_i64_i32 v[82:83], s[36:37], v82, s34, 0
	v_mad_i64_i32 v[88:89], s[36:37], v88, s34, 0
	v_mad_i64_i32 v[90:91], s[36:37], v90, s34, 0
	v_mad_i64_i32 v[96:97], s[36:37], v96, s34, 0
	v_mad_i64_i32 v[98:99], s[36:37], v98, s34, 0
	v_mad_i64_i32 v[104:105], s[36:37], v104, s34, 0
	v_mad_i64_i32 v[106:107], s[36:37], v106, s34, 0
	v_mad_i64_i32 v[112:113], s[36:37], v112, s34, 0
	v_mad_i64_i32 v[114:115], s[36:37], v114, s34, 0
	v_mad_i64_i32 v[120:121], s[36:37], v120, s34, 0
	v_mad_i64_i32 v[122:123], s[34:35], v122, s34, 0
	v_lshl_add_u64 v[56:57], v[56:57], 2, s[22:23]
	s_lshl_b64 s[2:3], s[20:21], 2
	v_lshl_add_u64 v[58:59], v[58:59], 2, s[22:23]
	v_lshl_add_u64 v[72:73], v[72:73], 2, s[22:23]
	v_lshl_add_u64 v[74:75], v[74:75], 2, s[22:23]
	v_lshl_add_u64 v[80:81], v[80:81], 2, s[22:23]
	v_lshl_add_u64 v[82:83], v[82:83], 2, s[22:23]
	v_lshl_add_u64 v[88:89], v[88:89], 2, s[22:23]
	v_lshl_add_u64 v[90:91], v[90:91], 2, s[22:23]
	v_lshl_add_u64 v[96:97], v[96:97], 2, s[22:23]
	v_lshl_add_u64 v[98:99], v[98:99], 2, s[22:23]
	v_lshl_add_u64 v[104:105], v[104:105], 2, s[22:23]
	v_lshl_add_u64 v[106:107], v[106:107], 2, s[22:23]
	v_lshl_add_u64 v[112:113], v[112:113], 2, s[22:23]
	v_lshl_add_u64 v[114:115], v[114:115], 2, s[22:23]
	v_lshl_add_u64 v[120:121], v[120:121], 2, s[22:23]
	v_lshl_add_u64 v[122:123], v[122:123], 2, s[22:23]
	v_lshl_add_u64 v[56:57], v[56:57], 0, s[2:3]
	v_lshl_add_u64 v[58:59], v[58:59], 0, s[2:3]
	v_lshl_add_u64 v[72:73], v[72:73], 0, s[2:3]
	v_lshl_add_u64 v[74:75], v[74:75], 0, s[2:3]
	v_lshl_add_u64 v[80:81], v[80:81], 0, s[2:3]
	v_lshl_add_u64 v[82:83], v[82:83], 0, s[2:3]
	v_lshl_add_u64 v[88:89], v[88:89], 0, s[2:3]
	v_lshl_add_u64 v[90:91], v[90:91], 0, s[2:3]
	v_lshl_add_u64 v[96:97], v[96:97], 0, s[2:3]
	v_lshl_add_u64 v[98:99], v[98:99], 0, s[2:3]
	v_lshl_add_u64 v[104:105], v[104:105], 0, s[2:3]
	v_lshl_add_u64 v[106:107], v[106:107], 0, s[2:3]
	v_lshl_add_u64 v[112:113], v[112:113], 0, s[2:3]
	v_lshl_add_u64 v[114:115], v[114:115], 0, s[2:3]
	v_lshl_add_u64 v[120:121], v[120:121], 0, s[2:3]
	v_lshl_add_u64 v[122:123], v[122:123], 0, s[2:3]
	v_lshl_add_u64 v[56:57], v[56:57], 0, v[128:129]
	v_lshl_add_u64 v[60:61], v[58:59], 0, v[128:129]
	v_lshl_add_u64 v[72:73], v[72:73], 0, v[128:129]
	s_waitcnt vmcnt(17)
	v_lshl_add_u64 v[76:77], v[74:75], 0, v[128:129]
	v_lshl_add_u64 v[80:81], v[80:81], 0, v[128:129]
	v_lshl_add_u64 v[84:85], v[82:83], 0, v[128:129]
	v_lshl_add_u64 v[88:89], v[88:89], 0, v[128:129]
	v_lshl_add_u64 v[92:93], v[90:91], 0, v[128:129]
	v_lshl_add_u64 v[96:97], v[96:97], 0, v[128:129]
	v_lshl_add_u64 v[100:101], v[98:99], 0, v[128:129]
	v_lshl_add_u64 v[104:105], v[104:105], 0, v[128:129]
	v_lshl_add_u64 v[108:109], v[106:107], 0, v[128:129]
	v_lshl_add_u64 v[112:113], v[112:113], 0, v[128:129]
	v_lshl_add_u64 v[116:117], v[114:115], 0, v[128:129]
	v_lshl_add_u64 v[120:121], v[120:121], 0, v[128:129]
	v_lshl_add_u64 v[124:125], v[122:123], 0, v[128:129]
	global_load_dwordx4 v[56:59], v[56:57], off nt
	s_nop 0
	global_load_dwordx4 v[60:63], v[60:61], off nt
	s_nop 0
	global_load_dwordx4 v[72:75], v[72:73], off nt
	s_nop 0
	global_load_dwordx4 v[76:79], v[76:77], off nt
	s_nop 0
	global_load_dwordx4 v[80:83], v[80:81], off nt
	s_nop 0
	global_load_dwordx4 v[84:87], v[84:85], off nt
	s_nop 0
	global_load_dwordx4 v[88:91], v[88:89], off nt
	s_nop 0
	global_load_dwordx4 v[92:95], v[92:93], off nt
	s_nop 0
	global_load_dwordx4 v[96:99], v[96:97], off nt
	s_nop 0
	global_load_dwordx4 v[100:103], v[100:101], off nt
	s_nop 0
	global_load_dwordx4 v[104:107], v[104:105], off nt
	s_nop 0
	global_load_dwordx4 v[108:111], v[108:109], off nt
	s_nop 0
	global_load_dwordx4 v[112:115], v[112:113], off nt
	s_nop 0
	global_load_dwordx4 v[116:119], v[116:117], off nt
	s_nop 0
	global_load_dwordx4 v[120:123], v[120:121], off nt
	s_nop 0
	global_load_dwordx4 v[124:127], v[124:125], off nt
	ds_write2_b32 v149, v4, v5 offset1:1
	ds_write2_b32 v149, v6, v7 offset0:2 offset1:3
	v_add_u32_e32 v4, 0x420, v149
	ds_write2_b32 v4, v0, v1 offset1:1
	v_add_u32_e32 v0, 0x428, v149
	ds_write2_b32 v0, v2, v3 offset1:1
	v_add_u32_e32 v0, 0x840, v149
	ds_write2_b32 v0, v12, v13 offset1:1
	v_add_u32_e32 v0, 0x848, v149
	ds_write2_b32 v0, v14, v15 offset1:1
; #define LAS __attribute__((address_space(3)))
; DI unsigned pk4f8(float a, float b, float c, float d) { int p = __builtin_amdgcn_cvt_pk_fp8_f32(a, b, 0, false); p = __builtin_amdgcn_cvt_pk_fp8_f32(c, d, p, true); return (unsigned)p; }
; DI void cv_finish(const CvItem& cc, int lane, LAS float* scr, const f32x4 (&v)[16]) {
;     { const int c4 = (lane & 7) * 4, r8 = lane >> 3;
; #pragma unroll
;       for (int i = 0; i < 16; ++i) { LAS float* d = scr + (8 * i + r8) * 33 + c4; d[0] = v[i][0]; d[1] = v[i][1]; d[2] = v[i][2]; d[3] = v[i][3]; } }
;     asm volatile("s_waitcnt lgkmcnt(0)" ::: "memory");
;     const int c = lane & 7;
; #pragma unroll
;     for (int j = 0; j < 4; ++j) { const int n = (lane >> 3) + 8 * j; const int src = cc.n0 + n; int dst = src;
;         if (cc.kind == 2) { const int jj = src & 2047; dst = (jj >> 7) * 256 + (src >> 11) * 128 + (jj & 127); }
;         const LAS float* sp = scr + (16 * c) * 33 + n;
;         u32x4 o; o.x = pk4f8(sp[0 * 33] * WSCALE, sp[1 * 33] * WSCALE, sp[2 * 33] * WSCALE, sp[3 * 33] * WSCALE); o.y = pk4f8(sp[4 * 33] * WSCALE, sp[5 * 33] * WSCALE, sp[6 * 33] * WSCALE, sp[7 * 33] * WSCALE);
;         o.z = pk4f8(sp[8 * 33] * WSCALE, sp[9 * 33] * WSCALE, sp[10 * 33] * WSCALE, sp[11 * 33] * WSCALE); o.w = pk4f8(sp[12 * 33] * WSCALE, sp[13 * 33] * WSCALE, sp[14 * 33] * WSCALE, sp[15 * 33] * WSCALE);
;         *(u32x4*)(cc.WT + (size_t)dst * D + cc.k0 + 16 * c) = o; }
	v_add_u32_e32 v0, 0xc60, v149
	ds_write2_b32 v0, v8, v9 offset1:1
	v_add_u32_e32 v0, 0xc68, v149
	ds_write2_b32 v0, v10, v11 offset1:1
	v_add_u32_e32 v0, 0x1080, v149
	ds_write2_b32 v0, v20, v21 offset1:1
	v_add_u32_e32 v0, 0x1088, v149
	ds_write2_b32 v0, v22, v23 offset1:1
	v_add_u32_e32 v0, 0x14a0, v149
	ds_write2_b32 v0, v16, v17 offset1:1
	v_add_u32_e32 v0, 0x14a8, v149
	ds_write2_b32 v0, v18, v19 offset1:1
	v_add_u32_e32 v0, 0x18c0, v149
	ds_write2_b32 v0, v28, v29 offset1:1
	v_add_u32_e32 v0, 0x18c8, v149
	ds_write2_b32 v0, v30, v31 offset1:1
	v_add_u32_e32 v0, 0x1ce0, v149
	ds_write2_b32 v0, v24, v25 offset1:1
	v_add_u32_e32 v0, 0x1ce8, v149
	ds_write2_b32 v0, v26, v27 offset1:1
	v_add_u32_e32 v0, 0x2100, v149
	ds_write2_b32 v0, v36, v37 offset1:1
	v_add_u32_e32 v0, 0x2108, v149
	ds_write2_b32 v0, v38, v39 offset1:1
	v_add_u32_e32 v0, 0x2520, v149
	ds_write2_b32 v0, v32, v33 offset1:1
	v_add_u32_e32 v0, 0x2528, v149
	ds_write2_b32 v0, v34, v35 offset1:1
	v_add_u32_e32 v0, 0x2940, v149
	ds_write2_b32 v0, v44, v45 offset1:1
	v_add_u32_e32 v0, 0x2948, v149
	ds_write2_b32 v0, v46, v47 offset1:1
	v_add_u32_e32 v0, 0x2d60, v149
	ds_write2_b32 v0, v40, v41 offset1:1
	v_add_u32_e32 v0, 0x2d68, v149
	ds_write2_b32 v0, v42, v43 offset1:1
	v_add_u32_e32 v0, 0x3180, v149
	ds_write2_b32 v0, v52, v53 offset1:1
	v_add_u32_e32 v0, 0x3188, v149
	ds_write2_b32 v0, v54, v55 offset1:1
	v_add_u32_e32 v0, 0x35a0, v149
	ds_write2_b32 v0, v48, v49 offset1:1
	v_add_u32_e32 v0, 0x35a8, v149
	ds_write2_b32 v0, v50, v51 offset1:1
	v_add_u32_e32 v0, 0x39c0, v149
	ds_write2_b32 v0, v68, v69 offset1:1
	v_add_u32_e32 v0, 0x39c8, v149
	ds_write2_b32 v0, v70, v71 offset1:1
	v_add_u32_e32 v0, 0x3de0, v149
	ds_write2_b32 v0, v64, v65 offset1:1
	v_add_u32_e32 v0, 0x3de8, v149
	ds_write2_b32 v0, v66, v67 offset1:1
	s_waitcnt lgkmcnt(0)
	v_add_u32_e32 v0, s12, v132
	v_lshlrev_b32_e32 v1, 1, v0
	v_ashrrev_i32_e32 v2, 4, v0
	ds_read2_b32 v[4:5], v148 offset1:8
	ds_read2_b32 v[6:7], v148 offset0:33 offset1:41
	ds_read2_b32 v[8:9], v148 offset0:66 offset1:74
	v_and_b32_e32 v1, 0xf00, v1
	v_and_b32_e32 v2, 0xffffff80, v2
	s_cmp_eq_u32 s11, 2
	v_add_u32_e32 v1, v1, v2
	v_and_or_b32 v1, v0, s27, v1
	s_cselect_b64 vcc, -1, 0
	ds_read2_b32 v[12:13], v148 offset0:99 offset1:107
	v_cndmask_b32_e32 v10, v0, v1, vcc
	s_waitcnt lgkmcnt(3)
	v_mul_f32_e32 v1, 0x44000000, v4
	s_waitcnt lgkmcnt(2)
	v_mul_f32_e32 v2, 0x44000000, v6
	v_mov_b32_e32 v0, v129
	v_cvt_pk_fp8_f32 v0, v1, v2
	ds_read2_b32 v[14:15], v148 offset0:132 offset1:140
	ds_read2_b32 v[16:17], v148 offset0:165 offset1:173
	ds_read2_b32 v[18:19], v148 offset0:198 offset1:206
	s_waitcnt lgkmcnt(4)
	v_mul_f32_e32 v3, 0x44000000, v8
	s_waitcnt lgkmcnt(3)
	v_mul_f32_e32 v1, 0x44000000, v12
	ds_read2_b32 v[20:21], v148 offset0:231 offset1:239
	v_add_u32_e32 v38, 0x400, v148
	v_cvt_pk_fp8_f32 v0, v3, v1 op_sel:[0,0,1]
	s_waitcnt lgkmcnt(3)
	v_mul_f32_e32 v2, 0x44000000, v14
	s_waitcnt lgkmcnt(2)
	v_mul_f32_e32 v3, 0x44000000, v16
	v_mov_b32_e32 v1, v129
	ds_read2_b32 v[22:23], v38 offset0:8 offset1:16
	v_cvt_pk_fp8_f32 v1, v2, v3
	ds_read2_b32 v[24:25], v38 offset0:41 offset1:49
	ds_read2_b32 v[26:27], v38 offset0:74 offset1:82
	ds_read2_b32 v[28:29], v38 offset0:107 offset1:115
	ds_read2_b32 v[30:31], v38 offset0:140 offset1:148
	ds_read2_b32 v[32:33], v38 offset0:173 offset1:181
	s_waitcnt lgkmcnt(7)
	v_mul_f32_e32 v4, 0x44000000, v18
	s_waitcnt lgkmcnt(6)
	v_mul_f32_e32 v2, 0x44000000, v20
	v_cvt_pk_fp8_f32 v1, v4, v2 op_sel:[0,0,1]
	s_waitcnt lgkmcnt(5)
	v_mul_f32_e32 v3, 0x44000000, v22
	s_waitcnt lgkmcnt(4)
	v_mul_f32_e32 v4, 0x44000000, v24
	v_mov_b32_e32 v2, v129
	ds_read2_b32 v[34:35], v38 offset0:206 offset1:214
	ds_read2_b32 v[36:37], v38 offset0:239 offset1:247
	v_cvt_pk_fp8_f32 v2, v3, v4
	s_waitcnt lgkmcnt(3)
	v_mul_f32_e32 v4, 0x44000000, v30
	s_waitcnt lgkmcnt(2)
	v_mul_f32_e32 v11, 0x44000000, v32
	v_mov_b32_e32 v3, v129
	v_cvt_pk_fp8_f32 v3, v4, v11
	v_mul_f32_e32 v6, 0x44000000, v26
	v_mul_f32_e32 v8, 0x44000000, v28
	v_cvt_pk_fp8_f32 v2, v6, v8 op_sel:[0,0,1]
	s_waitcnt lgkmcnt(1)
	v_mul_f32_e32 v4, 0x44000000, v34
	s_waitcnt lgkmcnt(0)
	v_mul_f32_e32 v6, 0x44000000, v36
	v_ashrrev_i32_e32 v11, 31, v10
	v_cvt_pk_fp8_f32 v3, v4, v6 op_sel:[0,0,1]
	v_lshlrev_b64 v[10:11], 11, v[10:11]
	v_lshl_add_u64 v[10:11], s[6:7], 0, v[10:11]
	s_ashr_i32 s11, s10, 31
	v_lshl_add_u64 v[10:11], v[10:11], 0, s[10:11]
	v_lshl_add_u64 v[10:11], v[10:11], 0, v[130:131]
	global_store_dwordx4 v[10:11], v[0:3], off
	v_mul_f32_e32 v6, 0x44000000, v17
	v_mul_f32_e32 v8, 0x44000000, v33
	v_add_u32_e32 v0, s12, v133
	v_lshlrev_b32_e32 v1, 1, v0
	v_ashrrev_i32_e32 v2, 4, v0
	v_and_b32_e32 v1, 0xf00, v1
	v_and_b32_e32 v2, 0xffffff80, v2
	v_add_u32_e32 v1, v1, v2
	v_and_or_b32 v1, v0, s27, v1
	v_cndmask_b32_e32 v4, v0, v1, vcc
	v_mul_f32_e32 v1, 0x44000000, v5
	v_mul_f32_e32 v2, 0x44000000, v7
	v_mov_b32_e32 v0, v129
	v_cvt_pk_fp8_f32 v0, v1, v2
	v_mul_f32_e32 v2, 0x44000000, v15
	v_mov_b32_e32 v1, v129
	v_cvt_pk_fp8_f32 v1, v2, v6
	v_mul_f32_e32 v3, 0x44000000, v9
	v_mul_f32_e32 v5, 0x44000000, v13
	v_cvt_pk_fp8_f32 v0, v3, v5 op_sel:[0,0,1]
	v_mul_f32_e32 v2, 0x44000000, v19
	v_mul_f32_e32 v3, 0x44000000, v21
	v_cvt_pk_fp8_f32 v1, v2, v3 op_sel:[0,0,1]
	v_mul_f32_e32 v3, 0x44000000, v23
	v_mul_f32_e32 v5, 0x44000000, v25
	v_mov_b32_e32 v2, v129
	v_cvt_pk_fp8_f32 v2, v3, v5
	v_mul_f32_e32 v5, 0x44000000, v31
	v_mov_b32_e32 v3, v129
	v_cvt_pk_fp8_f32 v3, v5, v8
	v_mul_f32_e32 v6, 0x44000000, v27
	v_mul_f32_e32 v7, 0x44000000, v29
	v_cvt_pk_fp8_f32 v2, v6, v7 op_sel:[0,0,1]
	v_mul_f32_e32 v5, 0x44000000, v35
	v_mul_f32_e32 v6, 0x44000000, v37
	v_cvt_pk_fp8_f32 v3, v5, v6 op_sel:[0,0,1]
	v_ashrrev_i32_e32 v5, 31, v4
	v_lshlrev_b64 v[4:5], 11, v[4:5]
	v_lshl_add_u64 v[4:5], s[6:7], 0, v[4:5]
	v_lshl_add_u64 v[4:5], v[4:5], 0, s[10:11]
	v_lshl_add_u64 v[4:5], v[4:5], 0, v[130:131]
	global_store_dwordx4 v[4:5], v[0:3], off
	ds_read2_b32 v[4:5], v148 offset0:16 offset1:24
	ds_read2_b32 v[6:7], v148 offset0:49 offset1:57
	ds_read2_b32 v[8:9], v148 offset0:82 offset1:90
	v_add_u32_e32 v0, s12, v134
	v_lshlrev_b32_e32 v1, 1, v0
	v_ashrrev_i32_e32 v2, 4, v0
	v_and_b32_e32 v1, 0xf00, v1
	v_and_b32_e32 v2, 0xffffff80, v2
	v_add_u32_e32 v1, v1, v2
	v_and_or_b32 v1, v0, s27, v1
	ds_read2_b32 v[12:13], v148 offset0:115 offset1:123
	v_cndmask_b32_e32 v10, v0, v1, vcc
	s_waitcnt lgkmcnt(3)
; #define LAS __attribute__((address_space(3)))
; DI unsigned pk4f8(float a, float b, float c, float d) { int p = __builtin_amdgcn_cvt_pk_fp8_f32(a, b, 0, false); p = __builtin_amdgcn_cvt_pk_fp8_f32(c, d, p, true); return (unsigned)p; }
; DI void cv_finish(const CvItem& cc, int lane, LAS float* scr, const f32x4 (&v)[16]) {
;     ...
; #pragma unroll
;     for (int j = 0; j < 4; ++j) { const int n = (lane >> 3) + 8 * j; const int src = cc.n0 + n; int dst = src;
;         if (cc.kind == 2) { const int jj = src & 2047; dst = (jj >> 7) * 256 + (src >> 11) * 128 + (jj & 127); }
;         const LAS float* sp = scr + (16 * c) * 33 + n;
;         u32x4 o; o.x = pk4f8(sp[0 * 33] * WSCALE, sp[1 * 33] * WSCALE, sp[2 * 33] * WSCALE, sp[3 * 33] * WSCALE); o.y = pk4f8(sp[4 * 33] * WSCALE, sp[5 * 33] * WSCALE, sp[6 * 33] * WSCALE, sp[7 * 33] * WSCALE);
;         o.z = pk4f8(sp[8 * 33] * WSCALE, sp[9 * 33] * WSCALE, sp[10 * 33] * WSCALE, sp[11 * 33] * WSCALE); o.w = pk4f8(sp[12 * 33] * WSCALE, sp[13 * 33] * WSCALE, sp[14 * 33] * WSCALE, sp[15 * 33] * WSCALE);
;         *(u32x4*)(cc.WT + (size_t)dst * D + cc.k0 + 16 * c) = o; }
;     asm volatile("s_waitcnt lgkmcnt(0)" ::: "memory");
; DI void conv_pool(const Params& P, LAS unsigned char* lds, int pool, int blk_lo, int blk_hi) {
;     ...
;         cv_finish(cur, lane, scr, v);
;         if (!more) break;
; #pragma unroll
;         for (int i = 0; i < 16; ++i) v[i] = vn[i];
;         cur = nxt; it = nx; }
	v_mul_f32_e32 v1, 0x44000000, v4
	s_waitcnt lgkmcnt(2)
	v_mul_f32_e32 v2, 0x44000000, v6
	v_mov_b32_e32 v0, v129
	ds_read2_b32 v[14:15], v148 offset0:148 offset1:156
	ds_read2_b32 v[16:17], v148 offset0:181 offset1:189
	v_cvt_pk_fp8_f32 v0, v1, v2
	s_waitcnt lgkmcnt(3)
	v_mul_f32_e32 v3, 0x44000000, v8
	s_waitcnt lgkmcnt(2)
	v_mul_f32_e32 v1, 0x44000000, v12
	ds_read2_b32 v[18:19], v148 offset0:214 offset1:222
	ds_read2_b32 v[20:21], v148 offset0:247 offset1:255
	v_cvt_pk_fp8_f32 v0, v3, v1 op_sel:[0,0,1]
	s_waitcnt lgkmcnt(3)
	v_mul_f32_e32 v2, 0x44000000, v14
	s_waitcnt lgkmcnt(2)
	v_mul_f32_e32 v3, 0x44000000, v16
	v_mov_b32_e32 v1, v129
	ds_read2_b32 v[22:23], v38 offset0:24 offset1:32
	v_cvt_pk_fp8_f32 v1, v2, v3
	ds_read2_b32 v[24:25], v38 offset0:57 offset1:65
	ds_read2_b32 v[26:27], v38 offset0:90 offset1:98
	ds_read2_b32 v[28:29], v38 offset0:123 offset1:131
	ds_read2_b32 v[30:31], v38 offset0:156 offset1:164
	ds_read2_b32 v[32:33], v38 offset0:189 offset1:197
	s_waitcnt lgkmcnt(7)
	v_mul_f32_e32 v4, 0x44000000, v18
	s_waitcnt lgkmcnt(6)
	v_mul_f32_e32 v2, 0x44000000, v20
	v_cvt_pk_fp8_f32 v1, v4, v2 op_sel:[0,0,1]
	s_waitcnt lgkmcnt(5)
	v_mul_f32_e32 v3, 0x44000000, v22
	s_waitcnt lgkmcnt(4)
	v_mul_f32_e32 v4, 0x44000000, v24
	v_mov_b32_e32 v2, v129
	v_cvt_pk_fp8_f32 v2, v3, v4
	v_add_u32_e32 v3, 0x600, v148
	ds_read2_b32 v[34:35], v38 offset0:222 offset1:230
	ds_read2_b32 v[36:37], v3 offset0:127 offset1:135
	s_waitcnt lgkmcnt(3)
	v_mul_f32_e32 v4, 0x44000000, v30
	s_waitcnt lgkmcnt(2)
	v_mul_f32_e32 v11, 0x44000000, v32
	v_mov_b32_e32 v3, v129
	v_cvt_pk_fp8_f32 v3, v4, v11
	v_mul_f32_e32 v6, 0x44000000, v26
	v_mul_f32_e32 v8, 0x44000000, v28
	v_cvt_pk_fp8_f32 v2, v6, v8 op_sel:[0,0,1]
	s_waitcnt lgkmcnt(1)
	v_mul_f32_e32 v4, 0x44000000, v34
	s_waitcnt lgkmcnt(0)
	v_mul_f32_e32 v6, 0x44000000, v36
	v_ashrrev_i32_e32 v11, 31, v10
	v_cvt_pk_fp8_f32 v3, v4, v6 op_sel:[0,0,1]
	v_lshlrev_b64 v[10:11], 11, v[10:11]
	v_lshl_add_u64 v[10:11], s[6:7], 0, v[10:11]
	v_lshl_add_u64 v[10:11], v[10:11], 0, s[10:11]
	v_lshl_add_u64 v[10:11], v[10:11], 0, v[130:131]
	global_store_dwordx4 v[10:11], v[0:3], off
	v_mul_f32_e32 v6, 0x44000000, v17
	v_mul_f32_e32 v8, 0x44000000, v33
	v_add_u32_e32 v0, s12, v135
	v_lshlrev_b32_e32 v1, 1, v0
	v_ashrrev_i32_e32 v2, 4, v0
	v_and_b32_e32 v1, 0xf00, v1
	v_and_b32_e32 v2, 0xffffff80, v2
	v_add_u32_e32 v1, v1, v2
	v_and_or_b32 v1, v0, s27, v1
	v_cndmask_b32_e32 v4, v0, v1, vcc
	v_mul_f32_e32 v1, 0x44000000, v5
	v_mul_f32_e32 v2, 0x44000000, v7
	v_mov_b32_e32 v0, v129
	v_cvt_pk_fp8_f32 v0, v1, v2
	v_mul_f32_e32 v2, 0x44000000, v15
	v_mov_b32_e32 v1, v129
	v_cvt_pk_fp8_f32 v1, v2, v6
	v_mul_f32_e32 v3, 0x44000000, v9
	v_mul_f32_e32 v5, 0x44000000, v13
	v_cvt_pk_fp8_f32 v0, v3, v5 op_sel:[0,0,1]
	v_mul_f32_e32 v2, 0x44000000, v19
	v_mul_f32_e32 v3, 0x44000000, v21
	v_cvt_pk_fp8_f32 v1, v2, v3 op_sel:[0,0,1]
	v_mul_f32_e32 v3, 0x44000000, v23
	v_mul_f32_e32 v5, 0x44000000, v25
	v_mov_b32_e32 v2, v129
	v_cvt_pk_fp8_f32 v2, v3, v5
	v_mul_f32_e32 v5, 0x44000000, v31
	v_mov_b32_e32 v3, v129
	v_cvt_pk_fp8_f32 v3, v5, v8
	v_mul_f32_e32 v6, 0x44000000, v27
	v_mul_f32_e32 v7, 0x44000000, v29
	v_cvt_pk_fp8_f32 v2, v6, v7 op_sel:[0,0,1]
	v_mul_f32_e32 v5, 0x44000000, v35
	v_mul_f32_e32 v6, 0x44000000, v37
	v_cvt_pk_fp8_f32 v3, v5, v6 op_sel:[0,0,1]
	v_ashrrev_i32_e32 v5, 31, v4
	v_lshlrev_b64 v[4:5], 11, v[4:5]
	v_lshl_add_u64 v[4:5], s[6:7], 0, v[4:5]
	v_lshl_add_u64 v[4:5], v[4:5], 0, s[10:11]
	v_lshl_add_u64 v[4:5], v[4:5], 0, v[130:131]
	global_store_dwordx4 v[4:5], v[0:3], off
	s_waitcnt lgkmcnt(0)
	s_waitcnt vmcnt(19)
	v_mov_b64_e32 v[4:5], v[56:57]
	s_waitcnt vmcnt(17)
	v_mov_b64_e32 v[12:13], v[72:73]
	v_mov_b64_e32 v[0:1], v[60:61]
	s_waitcnt vmcnt(16)
	v_mov_b64_e32 v[8:9], v[76:77]
	s_waitcnt vmcnt(15)
	v_mov_b64_e32 v[20:21], v[80:81]
	s_waitcnt vmcnt(14)
	v_mov_b64_e32 v[16:17], v[84:85]
	s_waitcnt vmcnt(13)
	v_mov_b64_e32 v[28:29], v[88:89]
	s_waitcnt vmcnt(12)
	v_mov_b64_e32 v[24:25], v[92:93]
	s_waitcnt vmcnt(11)
	v_mov_b64_e32 v[36:37], v[96:97]
	s_waitcnt vmcnt(10)
	v_mov_b64_e32 v[32:33], v[100:101]
	s_waitcnt vmcnt(9)
	v_mov_b64_e32 v[44:45], v[104:105]
	s_waitcnt vmcnt(8)
	v_mov_b64_e32 v[40:41], v[108:109]
	s_waitcnt vmcnt(7)
	v_mov_b64_e32 v[52:53], v[112:113]
	s_waitcnt vmcnt(6)
	v_mov_b64_e32 v[48:49], v[116:117]
	s_waitcnt vmcnt(5)
	v_mov_b64_e32 v[68:69], v[120:121]
	s_waitcnt vmcnt(4)
	v_mov_b64_e32 v[64:65], v[124:125]
	s_andn2_b64 vcc, exec, s[18:19]
	v_mov_b64_e32 v[6:7], v[58:59]
	v_mov_b64_e32 v[2:3], v[62:63]
	v_mov_b64_e32 v[14:15], v[74:75]
	v_mov_b64_e32 v[10:11], v[78:79]
	v_mov_b64_e32 v[22:23], v[82:83]
	v_mov_b64_e32 v[18:19], v[86:87]
	v_mov_b64_e32 v[30:31], v[90:91]
	v_mov_b64_e32 v[26:27], v[94:95]
	v_mov_b64_e32 v[38:39], v[98:99]
	v_mov_b64_e32 v[34:35], v[102:103]
	v_mov_b64_e32 v[46:47], v[106:107]
	v_mov_b64_e32 v[42:43], v[110:111]
	v_mov_b64_e32 v[54:55], v[114:115]
	v_mov_b64_e32 v[50:51], v[118:119]
	v_mov_b64_e32 v[70:71], v[122:123]
	v_mov_b64_e32 v[66:67], v[126:127]
	s_mov_b64 s[6:7], s[16:17]
	s_mov_b32 s11, s14
	s_mov_b32 s10, s33
	s_mov_b32 s12, s20
	s_mov_b32 s20, s29
	s_mov_b32 s14, s28
	s_cbranch_vccz .LBB0_1136
